# ph_light: the two 64-lane sum-of-squares reductions use DPP row operations (quad_perm / row_mirror / row_bcast) instead of 12 serial ds_bpermute round trips
# speedup vs baseline: 1.0052x; 1.0011x over previous
.LBB0_293:
	s_or_b64 exec, exec, s[28:29]
	s_waitcnt lgkmcnt(0)
	s_nop 4
	v_add_f32_dpp v1, v1, v1 quad_perm:[1,0,3,2] row_mask:0xf bank_mask:0xf
	v_add_f32_dpp v0, v0, v0 quad_perm:[1,0,3,2] row_mask:0xf bank_mask:0xf
	s_nop 0
	v_add_f32_dpp v1, v1, v1 quad_perm:[2,3,0,1] row_mask:0xf bank_mask:0xf
	v_add_f32_dpp v0, v0, v0 quad_perm:[2,3,0,1] row_mask:0xf bank_mask:0xf
	s_nop 0
	v_add_f32_dpp v1, v1, v1 row_half_mirror row_mask:0xf bank_mask:0xf
	v_add_f32_dpp v0, v0, v0 row_half_mirror row_mask:0xf bank_mask:0xf
	s_nop 0
	v_add_f32_dpp v1, v1, v1 row_mirror row_mask:0xf bank_mask:0xf
	v_add_f32_dpp v0, v0, v0 row_mirror row_mask:0xf bank_mask:0xf
	s_nop 0
	v_add_f32_dpp v1, v1, v1 row_bcast:15 row_mask:0xa bank_mask:0xf
	v_add_f32_dpp v0, v0, v0 row_bcast:15 row_mask:0xa bank_mask:0xf
	s_nop 0
	v_add_f32_dpp v1, v1, v1 row_bcast:31 row_mask:0xc bank_mask:0xf
	v_add_f32_dpp v0, v0, v0 row_bcast:31 row_mask:0xc bank_mask:0xf
	s_nop 0
	s_nop 1
	v_readlane_b32 s30, v1, 63
	v_readlane_b32 s31, v0, 63
	s_and_saveexec_b64 s[28:29], s[14:15]
	s_cbranch_execz .LBB0_276
	s_nop 1
	v_mov_b32_e32 v0, s30
	v_mov_b32_e32 v1, s31
	v_fmamk_f32 v0, v0, 0x3b2aaaab, v204
	v_fmamk_f32 v1, v1, 0x3b800000, v204
	v_rsq_f32_e32 v0, v0
	v_rsq_f32_e32 v1, v1
	flat_store_dword v[22:23], v0
	flat_store_dword v[24:25], v1
	s_branch .LBB0_276
.LBB0_295:
	s_or_b64 exec, exec, s[16:17]
	s_mov_b32 s0, s37
	s_mov_b32 s1, s33
	v_mbcnt_lo_u32_b32 v0, -1, s0
	v_mbcnt_hi_u32_b32 v0, -1, v0
	v_lshl_or_b32 v0, s1, 6, v0
	v_readlane_b32 s0, v254, 0
	s_mov_b32 s8, s0
	s_mov_b32 s0, s37
	s_add_i32 s0, s0, 0x20120
	v_mov_b32_e32 v1, s0
	v_readlane_b32 s1, v254, 1
	s_waitcnt lgkmcnt(0)
	ds_read_b64 v[2:3], v1
	s_mov_b32 s1, 0
	s_add_i32 s1, s1, 0x20040
	v_mov_b32_e32 v1, s1
	s_waitcnt lgkmcnt(0)
	v_readfirstlane_b32 s0, v3
	v_readfirstlane_b32 s2, v2
	ds_read_b64 v[2:3], v1
	s_mov_b32 s6, s60
	s_mov_b32 s5, 0
	s_add_i32 s5, s5, 0x20048
	v_mov_b32_e32 v1, s5
	s_waitcnt lgkmcnt(0)
	v_readfirstlane_b32 s1, v3
	v_readfirstlane_b32 s4, v2
	ds_read_b64 v[2:3], v1
	s_mov_b32 s14, s60
	s_mov_b32 s9, 0
	s_add_i32 s9, s9, 0x20050
	v_mov_b32_e32 v1, s9
	s_waitcnt lgkmcnt(0)
	v_readfirstlane_b32 s5, v3
	v_readfirstlane_b32 s7, v2
	ds_read_b64 v[2:3], v1
	s_mov_b32 s18, s60
	s_mov_b32 s9, 0
	s_add_i32 s9, s9, 0x20058
	v_mov_b32_e32 v1, s9
	s_waitcnt lgkmcnt(0)
	v_readfirstlane_b32 s17, v3
	v_readfirstlane_b32 s16, v2
	ds_read_b64 v[2:3], v1
	s_mov_b32 s22, s60
	s_mov_b32 s9, 0
	s_add_i32 s9, s9, 0x20060
	v_mov_b32_e32 v1, s9
	s_waitcnt lgkmcnt(0)
	v_readfirstlane_b32 s19, v3
	v_readfirstlane_b32 s20, v2
	ds_read_b64 v[2:3], v1
	s_mov_b32 s24, s60
	s_mov_b32 s9, 0
	s_add_i32 s9, s9, 0x20120
	v_mov_b32_e32 v1, s9
	s_waitcnt lgkmcnt(0)
	v_readfirstlane_b32 s21, v3
	v_readfirstlane_b32 s23, v2
	ds_read_b64 v[2:3], v1
	v_ashrrev_i32_e32 v1, 6, v0
	v_lshl_add_u32 v9, s8, 3, v1
	s_cmpk_lt_u32 s8, 0xc0
	s_cselect_b32 s30, 1, 0
	v_add_u32_e32 v4, 0x600, v9
	s_movk_i32 s31, 0x6ff
	v_cmp_lt_u32_e32 vcc, s31, v9
	s_nop 1
	v_cndmask_b32_e32 v9, v9, v4, vcc
	s_movk_i32 s8, 0xe00
	v_cmp_gt_i32_e32 vcc, s8, v9
	s_waitcnt lgkmcnt(0)
	v_readfirstlane_b32 s25, v3
	v_readfirstlane_b32 s26, v2
	s_and_saveexec_b64 s[8:9], vcc
	s_cbranch_execz .LBB0_308
	s_add_u32 s10, s2, 0x8003600
	s_addc_u32 s11, s0, 0
	s_mul_hi_i32 s0, s6, 0x1c00
	s_mulk_i32 s6, 0x1c00
	s_add_u32 s12, s4, s6
	s_addc_u32 s13, s1, s0
	s_mul_hi_i32 s0, s14, 0x1c00
	s_mulk_i32 s14, 0x1c00
	s_add_u32 s14, s7, s14
	s_addc_u32 s15, s5, s0
	s_mul_hi_i32 s0, s18, 0x70
	s_mulk_i32 s18, 0x70
	s_add_u32 s16, s16, s18
	s_addc_u32 s17, s17, s0
	s_mul_hi_i32 s0, s22, 0x1c000
	s_mul_i32 s22, s22, 0x1c000
	s_add_u32 s18, s20, s22
	s_addc_u32 s19, s19, s0
	s_mul_hi_i32 s0, s24, 0x1c000
	s_mul_i32 s24, s24, 0x1c000
	s_add_u32 s20, s23, s24
	s_addc_u32 s21, s21, s0
	v_and_b32_e32 v8, 63, v0
	s_add_u32 s22, s26, 0x1944b600
	v_lshl_add_u32 v54, v1, 11, 0
	v_lshlrev_b32_e32 v0, 5, v8
	s_addc_u32 s23, s25, 0
	v_mul_hi_u32_u24_e32 v11, 0x20c0, v8
	v_mul_u32_u24_e32 v10, 0x20c0, v8
	s_mov_b64 s[24:25], 0
	v_add_u32_e32 v55, v54, v0
	v_lshlrev_b32_e32 v144, 2, v8
.LBB0_297:
	v_ashrrev_i32_e32 v0, 31, v9
	v_lshrrev_b32_e32 v0, 27, v0
	v_add_u32_e32 v0, v9, v0
	v_ashrrev_i32_e32 v12, 5, v0
	v_mul_hi_i32 v0, v12, s78
	v_add_u32_e32 v0, v0, v12
	v_lshrrev_b32_e32 v1, 31, v0
	v_ashrrev_i32_e32 v0, 4, v0
	v_add_u32_e32 v0, v0, v1
	v_mov_b32_e32 v92, v0
	v_mul_lo_u32 v0, v0, 28
	v_sub_u32_e32 v0, v12, v0
	v_ashrrev_i32_e32 v1, 31, v0
	v_lshl_add_u64 v[2:3], v[0:1], 2, s[16:17]
	global_load_dword v1, v[2:3], off
	v_lshl_or_b32 v4, v0, 6, v8
	v_ashrrev_i32_e32 v5, 31, v4
	v_lshlrev_b64 v[6:7], 2, v[4:5]
	v_lshl_add_u64 v[2:3], s[14:15], 0, v[6:7]
	global_load_dword v3, v[2:3], off
	v_lshl_add_u64 v[6:7], s[12:13], 0, v[6:7]
	global_load_dword v2, v[6:7], off
	v_lshlrev_b64 v[88:89], 6, v[4:5]
	v_lshl_add_u64 v[90:91], s[18:19], 0, v[88:89]
	v_lshl_add_u64 v[88:89], s[20:21], 0, v[88:89]
	global_load_dwordx4 v[96:99], v[90:91], off
	global_load_dwordx4 v[100:103], v[88:89], off
	global_load_dwordx4 v[104:107], v[90:91], off offset:16
	global_load_dwordx4 v[108:111], v[88:89], off offset:16
	global_load_dwordx4 v[112:115], v[90:91], off offset:32
	global_load_dwordx4 v[116:119], v[88:89], off offset:32
	global_load_dwordx4 v[120:123], v[90:91], off offset:48
	global_load_dwordx4 v[124:127], v[88:89], off offset:48
	v_lshlrev_b32_e32 v93, 5, v12
	v_sub_u32_e32 v93, v9, v93
	v_mov_b64_e32 v[94:95], s[10:11]
	s_mov_b32 s4, 0x1060000
	s_mov_b32 s5, 0x83000
	v_mad_i64_i32 v[94:95], s[6:7], v92, s4, v[94:95]
	v_mad_i64_i32 v[94:95], s[6:7], v93, s5, v[94:95]
	v_lshlrev_b32_e32 v92, 5, v0
	v_mov_b32_e32 v93, 0
	v_lshl_add_u64 v[94:95], v[92:93], 0, v[94:95]
	v_lshl_add_u64 v[94:95], v[94:95], 0, v[10:11]
	v_mov_b64_e32 v[202:203], v[94:95]
	global_load_dwordx4 v[128:131], v[94:95], off offset:2688
	global_load_dwordx4 v[132:135], v[94:95], off offset:2704
	v_lshlrev_b32_e32 v138, 1, v54
	v_lshl_add_u32 v137, v8, 6, v138
	s_waitcnt vmcnt(10) lgkmcnt(0)
	v_mul_f32_e32 v5, 0x3fb8aa3b, v1
	v_fma_f32 v6, v1, s81, -v5
	v_rndne_f32_e32 v7, v5
	v_fmac_f32_e32 v6, 0x32a5705f, v1
	v_sub_f32_e32 v5, v5, v7
	v_add_f32_e32 v5, v5, v6
	v_cvt_i32_f32_e32 v7, v7
	v_exp_f32_e32 v5, v5
	v_cmp_ngt_f32_e32 vcc, s86, v1
	v_ldexp_f32 v5, v5, v7
	s_nop 0
	v_cndmask_b32_e32 v5, 0, v5, vcc
	v_cmp_nlt_f32_e32 vcc, s92, v1
	s_nop 1
	v_cndmask_b32_e32 v1, v221, v5, vcc
	v_mul_f32_e32 v5, v3, v1
	v_and_b32_e32 v6, 0x7fffffff, v5
	v_lshrrev_b32_e32 v7, 23, v6
	v_and_b32_e32 v13, 0x7fffff, v6
	v_cmp_nlt_f32_e64 s[26:27], |v5|, s87
	v_add_u32_e32 v15, 0xffffff88, v7
	v_or_b32_e32 v14, 0x800000, v13
	s_and_saveexec_b64 s[0:1], s[26:27]
	s_xor_b64 s[28:29], exec, s[0:1]
	s_cbranch_execz .LBB0_299
	v_cmp_lt_u32_e32 vcc, 63, v15
	v_not_b32_e32 v16, 31
	v_mov_b32_e32 v19, v145
	v_cndmask_b32_e32 v7, 0, v223, vcc
	v_add_u32_e32 v7, v7, v15
	v_cmp_lt_u32_e64 s[0:1], 31, v7
	v_mov_b32_e32 v21, v145
	v_mov_b32_e32 v23, v145
	v_cndmask_b32_e64 v13, 0, v16, s[0:1]
	v_add_u32_e32 v7, v13, v7
	v_cmp_lt_u32_e64 s[4:5], 31, v7
	v_mov_b32_e32 v25, v145
	s_mov_b32 s2, 0xfc2757d1
	v_cndmask_b32_e64 v13, 0, v16, s[4:5]
	v_mad_u64_u32 v[16:17], s[6:7], v14, s88, 0
	v_mov_b32_e32 v18, v17
	v_mad_u64_u32 v[18:19], s[6:7], v14, s89, v[18:19]
	v_mov_b32_e32 v20, v19
	v_mad_u64_u32 v[20:21], s[6:7], v14, s90, v[20:21]
	v_mov_b32_e32 v22, v21
	v_mad_u64_u32 v[22:23], s[6:7], v14, s91, v[22:23]
	v_mov_b32_e32 v24, v23
	v_mad_u64_u32 v[24:25], s[6:7], v14, s2, v[24:25]
	v_mov_b32_e32 v26, v25
	v_mov_b32_e32 v27, v145
	s_mov_b32 s2, 0x4e441529
	v_mad_u64_u32 v[26:27], s[6:7], v14, s2, v[26:27]
	v_mov_b32_e32 v28, v27
	v_mov_b32_e32 v29, v145
	s_mov_b32 s2, 0xa2f9836e
	v_mad_u64_u32 v[28:29], s[6:7], v14, s2, v[28:29]
	v_add_u32_e32 v7, v13, v7
	v_cndmask_b32_e32 v13, v26, v22, vcc
	v_cndmask_b32_e32 v17, v28, v24, vcc
	v_cndmask_b32_e32 v21, v29, v26, vcc
	v_cndmask_b32_e64 v19, v17, v13, s[0:1]
	v_cndmask_b32_e64 v17, v21, v17, s[0:1]
	v_cndmask_b32_e32 v21, v24, v20, vcc
	v_cndmask_b32_e64 v13, v13, v21, s[0:1]
	v_cndmask_b32_e64 v17, v17, v19, s[4:5]
	v_cndmask_b32_e64 v19, v19, v13, s[4:5]
	v_sub_u32_e32 v23, 32, v7
	v_alignbit_b32 v24, v17, v19, v23
	v_cmp_eq_u32_e64 s[6:7], 0, v7
	v_cndmask_b32_e32 v16, v20, v16, vcc
	s_nop 0
	v_cndmask_b32_e64 v7, v24, v17, s[6:7]
	v_cndmask_b32_e32 v17, v22, v18, vcc
	v_cndmask_b32_e64 v18, v21, v17, s[0:1]
	v_cndmask_b32_e64 v13, v13, v18, s[4:5]
	v_alignbit_b32 v21, v19, v13, v23
	v_cndmask_b32_e64 v19, v21, v19, s[6:7]
	v_bfe_u32 v24, v7, 29, 1
	v_cndmask_b32_e64 v16, v17, v16, s[0:1]
	v_alignbit_b32 v21, v7, v19, 30
	v_sub_u32_e32 v25, 0, v24
	v_cndmask_b32_e64 v16, v18, v16, s[4:5]
	v_xor_b32_e32 v21, v21, v25
	v_alignbit_b32 v17, v13, v16, v23
	v_cndmask_b32_e64 v13, v17, v13, s[6:7]
	v_ffbh_u32_e32 v18, v21
	v_alignbit_b32 v17, v19, v13, 30
	v_min_u32_e32 v18, 32, v18
	v_alignbit_b32 v13, v13, v16, 30
	v_xor_b32_e32 v17, v17, v25
	v_sub_u32_e32 v19, 31, v18
	v_xor_b32_e32 v13, v13, v25
	v_alignbit_b32 v20, v21, v17, v19
	v_alignbit_b32 v13, v17, v13, v19
	v_alignbit_b32 v16, v20, v13, 9
	v_ffbh_u32_e32 v17, v16
	v_min_u32_e32 v17, 32, v17
	v_lshrrev_b32_e32 v22, 29, v7
	v_not_b32_e32 v19, v17
	v_alignbit_b32 v13, v16, v13, v19
	v_lshlrev_b32_e32 v16, 31, v22
	v_or_b32_e32 v19, 0x33000000, v16
	v_add_lshl_u32 v17, v17, v18, 23
	v_lshrrev_b32_e32 v13, 9, v13
	v_sub_u32_e32 v17, v19, v17
	v_or_b32_e32 v16, 0.5, v16
	v_lshlrev_b32_e32 v18, 23, v18
	v_or_b32_e32 v13, v17, v13
	v_lshrrev_b32_e32 v17, 9, v20
	v_sub_u32_e32 v16, v16, v18
	v_or_b32_e32 v16, v17, v16
	v_mul_f32_e32 v17, 0x3fc90fda, v16
	s_mov_b32 s0, 0x3fc90fda
	v_fma_f32 v18, v16, s0, -v17
	v_fmac_f32_e32 v18, 0x33a22168, v16
	v_fmac_f32_e32 v18, 0x3fc90fda, v13
	v_lshrrev_b32_e32 v7, 30, v7
	v_add_f32_e32 v13, v17, v18
	v_add_u32_e32 v7, v24, v7

.Lssml_stage:
	s_waitcnt vmcnt(0)
	v_lshlrev_b32_e32 v146, 16, v128
	v_and_b32_e32 v147, 0xffff0000, v128
	v_lshlrev_b32_e32 v148, 16, v129
	v_and_b32_e32 v149, 0xffff0000, v129
	v_lshlrev_b32_e32 v150, 16, v130
	v_and_b32_e32 v151, 0xffff0000, v130
	v_lshlrev_b32_e32 v152, 16, v131
	v_and_b32_e32 v153, 0xffff0000, v131
	v_lshlrev_b32_e32 v154, 16, v132
	v_and_b32_e32 v155, 0xffff0000, v132
	v_lshlrev_b32_e32 v156, 16, v133
	v_and_b32_e32 v157, 0xffff0000, v133
	v_lshlrev_b32_e32 v158, 16, v134
	v_and_b32_e32 v159, 0xffff0000, v134
	v_lshlrev_b32_e32 v160, 16, v135
	v_and_b32_e32 v161, 0xffff0000, v135
	ds_write_b128 v137, v[146:149]
	ds_write_b128 v137, v[150:153] offset:16
	ds_write_b128 v137, v[154:157] offset:32
	ds_write_b128 v137, v[158:161] offset:48
	v_mov_b32_e32 v51, v57
	s_waitcnt lgkmcnt(0)
	s_cmp_eq_u32 s30, 2
	s_cbranch_scc1 .Lssml_sb0
	s_mul_i32 s4, s33, 0x2100
	s_add_i32 s4, s4, 0x8000
	v_lshl_add_u32 v140, v8, 3, s4
	v_and_b32_e32 v139, 15, v8
	v_lshrrev_b32_e32 v143, 4, v8
	v_lshlrev_b32_e32 v139, 2, v139
	v_mul_u32_u24_e32 v141, 0x210, v143
	v_mul_u32_u24_e32 v142, 0x840, v143
	v_add3_u32 v141, v141, v139, s4
	v_add3_u32 v142, v142, v139, s4
	v_lshlrev_b32_e32 v139, 4, v139
	v_lshl_add_u32 v143, v143, 2, v139
	v_add_u32_e32 v143, v143, v138
	ds_write_b64 v140, v[20:21]
	ds_write_b64 v140, v[22:23] offset:528
	ds_write_b64 v140, v[24:25] offset:1056
	ds_write_b64 v140, v[26:27] offset:1584
	ds_write_b64 v140, v[28:29] offset:2112
	ds_write_b64 v140, v[30:31] offset:2640
	ds_write_b64 v140, v[32:33] offset:3168
	ds_write_b64 v140, v[34:35] offset:3696
	ds_write_b64 v140, v[36:37] offset:4224
	ds_write_b64 v140, v[38:39] offset:4752
	ds_write_b64 v140, v[40:41] offset:5280
	ds_write_b64 v140, v[42:43] offset:5808
	ds_write_b64 v140, v[44:45] offset:6336
	ds_write_b64 v140, v[46:47] offset:6864
	ds_write_b64 v140, v[48:49] offset:7392
	ds_write_b64 v140, v[50:51] offset:7920
	s_waitcnt lgkmcnt(0)
	ds_read_b32 v56, v141
	ds_read_b32 v57, v141 offset:64
	ds_read_b32 v58, v141 offset:128
	ds_read_b32 v59, v141 offset:192
	ds_read_b32 v60, v141 offset:256
	ds_read_b32 v61, v141 offset:320
	ds_read_b32 v62, v141 offset:384
	ds_read_b32 v63, v141 offset:448
	ds_read_b32 v64, v141 offset:2112
	ds_read_b32 v65, v141 offset:2176
	ds_read_b32 v66, v141 offset:2240
	ds_read_b32 v67, v141 offset:2304
	ds_read_b32 v68, v141 offset:2368
	ds_read_b32 v69, v141 offset:2432
	ds_read_b32 v70, v141 offset:2496
	ds_read_b32 v71, v141 offset:2560
	ds_read_b32 v72, v141 offset:4224
	ds_read_b32 v73, v141 offset:4288
	ds_read_b32 v74, v141 offset:4352
	ds_read_b32 v75, v141 offset:4416
	ds_read_b32 v76, v141 offset:4480
	ds_read_b32 v77, v141 offset:4544
	ds_read_b32 v78, v141 offset:4608
	ds_read_b32 v79, v141 offset:4672
	ds_read_b32 v80, v141 offset:6336
	ds_read_b32 v81, v141 offset:6400
	ds_read_b32 v82, v141 offset:6464
	ds_read_b32 v83, v141 offset:6528
	ds_read_b32 v84, v141 offset:6592
	ds_read_b32 v85, v141 offset:6656
	ds_read_b32 v86, v141 offset:6720
	ds_read_b32 v87, v141 offset:6784
.Lssml_sb0:
	ds_read_b32 v88, v143
	ds_read_b32 v89, v143 offset:16
	ds_read_b32 v90, v143 offset:32
	ds_read_b32 v91, v143 offset:48
	s_waitcnt lgkmcnt(0)
	v_mfma_f32_16x16x4_f32 v[92:95], v88, v56, 0
	v_mfma_f32_16x16x4_f32 v[96:99], v88, v57, 0
	v_mfma_f32_16x16x4_f32 v[100:103], v88, v58, 0
	v_mfma_f32_16x16x4_f32 v[104:107], v88, v59, 0
	v_mfma_f32_16x16x4_f32 v[108:111], v88, v60, 0
	v_mfma_f32_16x16x4_f32 v[112:115], v88, v61, 0
	v_mfma_f32_16x16x4_f32 v[116:119], v88, v62, 0
	v_mfma_f32_16x16x4_f32 v[120:123], v88, v63, 0
	v_mfma_f32_16x16x4_f32 v[92:95], v89, v64, v[92:95]
	v_mfma_f32_16x16x4_f32 v[96:99], v89, v65, v[96:99]
	v_mfma_f32_16x16x4_f32 v[100:103], v89, v66, v[100:103]
	v_mfma_f32_16x16x4_f32 v[104:107], v89, v67, v[104:107]
	v_mfma_f32_16x16x4_f32 v[108:111], v89, v68, v[108:111]
	v_mfma_f32_16x16x4_f32 v[112:115], v89, v69, v[112:115]
	v_mfma_f32_16x16x4_f32 v[116:119], v89, v70, v[116:119]
	v_mfma_f32_16x16x4_f32 v[120:123], v89, v71, v[120:123]
	v_mfma_f32_16x16x4_f32 v[92:95], v90, v72, v[92:95]
	v_mfma_f32_16x16x4_f32 v[96:99], v90, v73, v[96:99]
	v_mfma_f32_16x16x4_f32 v[100:103], v90, v74, v[100:103]
	v_mfma_f32_16x16x4_f32 v[104:107], v90, v75, v[104:107]
	v_mfma_f32_16x16x4_f32 v[108:111], v90, v76, v[108:111]
	v_mfma_f32_16x16x4_f32 v[112:115], v90, v77, v[112:115]
	v_mfma_f32_16x16x4_f32 v[116:119], v90, v78, v[116:119]
	v_mfma_f32_16x16x4_f32 v[120:123], v90, v79, v[120:123]
	v_mfma_f32_16x16x4_f32 v[92:95], v91, v80, v[92:95]
	v_mfma_f32_16x16x4_f32 v[96:99], v91, v81, v[96:99]
	v_mfma_f32_16x16x4_f32 v[100:103], v91, v82, v[100:103]
	v_mfma_f32_16x16x4_f32 v[104:107], v91, v83, v[104:107]
	v_mfma_f32_16x16x4_f32 v[108:111], v91, v84, v[108:111]
	v_mfma_f32_16x16x4_f32 v[112:115], v91, v85, v[112:115]
	v_mfma_f32_16x16x4_f32 v[116:119], v91, v86, v[116:119]
	v_mfma_f32_16x16x4_f32 v[120:123], v91, v87, v[120:123]
	s_nop 15
	s_nop 7
	ds_write_b32 v142, v92
	ds_write_b32 v142, v93 offset:528
	ds_write_b32 v142, v94 offset:1056
	ds_write_b32 v142, v95 offset:1584
	ds_write_b32 v142, v96 offset:64
	ds_write_b32 v142, v97 offset:592
	ds_write_b32 v142, v98 offset:1120
	ds_write_b32 v142, v99 offset:1648
	ds_write_b32 v142, v100 offset:128
	ds_write_b32 v142, v101 offset:656
	ds_write_b32 v142, v102 offset:1184
	ds_write_b32 v142, v103 offset:1712
	ds_write_b32 v142, v104 offset:192
	ds_write_b32 v142, v105 offset:720
	ds_write_b32 v142, v106 offset:1248
	ds_write_b32 v142, v107 offset:1776
	ds_write_b32 v142, v108 offset:256
	ds_write_b32 v142, v109 offset:784
	ds_write_b32 v142, v110 offset:1312
	ds_write_b32 v142, v111 offset:1840
	ds_write_b32 v142, v112 offset:320
	ds_write_b32 v142, v113 offset:848
	ds_write_b32 v142, v114 offset:1376
	ds_write_b32 v142, v115 offset:1904
	ds_write_b32 v142, v116 offset:384
	ds_write_b32 v142, v117 offset:912
	ds_write_b32 v142, v118 offset:1440
	ds_write_b32 v142, v119 offset:1968
	ds_write_b32 v142, v120 offset:448
	ds_write_b32 v142, v121 offset:976
	ds_write_b32 v142, v122 offset:1504
	ds_write_b32 v142, v123 offset:2032
	ds_read_b32 v198, v143 offset:1024
	ds_read_b32 v199, v143 offset:1040
	ds_read_b32 v200, v143 offset:1056
	ds_read_b32 v201, v143 offset:1072
	s_waitcnt lgkmcnt(0)
	ds_read_b64 v[146:147], v140
	ds_read_b64 v[148:149], v140 offset:528
	ds_read_b64 v[150:151], v140 offset:1056
	ds_read_b64 v[152:153], v140 offset:1584
	ds_read_b64 v[154:155], v140 offset:2112
	ds_read_b64 v[156:157], v140 offset:2640
	ds_read_b64 v[158:159], v140 offset:3168
	ds_read_b64 v[160:161], v140 offset:3696
	ds_read_b64 v[162:163], v140 offset:4224
	ds_read_b64 v[164:165], v140 offset:4752
	ds_read_b64 v[166:167], v140 offset:5280
	ds_read_b64 v[168:169], v140 offset:5808
	ds_read_b64 v[170:171], v140 offset:6336
	ds_read_b64 v[172:173], v140 offset:6864
	ds_read_b64 v[174:175], v140 offset:7392
	ds_read_b64 v[176:177], v140 offset:7920
	s_waitcnt lgkmcnt(15)
	v_pk_fma_f32 v[146:147], v[18:19], v[52:53], v[146:147] op_sel:[0,1,0] op_sel_hi:[1,0,1]
	v_mfma_f32_16x16x4_f32 v[124:127], v198, v56, 0
	v_pk_fma_f32 v[52:53], v[16:17], v[52:53], v[146:147]
	v_mfma_f32_16x16x4_f32 v[128:131], v198, v57, 0
	s_waitcnt lgkmcnt(14)
	v_pk_fma_f32 v[148:149], v[18:19], v[52:53], v[148:149] op_sel:[0,1,0] op_sel_hi:[1,0,1]
	v_mfma_f32_16x16x4_f32 v[132:135], v198, v58, 0
	v_pk_fma_f32 v[52:53], v[16:17], v[52:53], v[148:149]
	v_mfma_f32_16x16x4_f32 v[178:181], v198, v59, 0
	s_waitcnt lgkmcnt(13)
	v_pk_fma_f32 v[150:151], v[18:19], v[52:53], v[150:151] op_sel:[0,1,0] op_sel_hi:[1,0,1]
	v_mfma_f32_16x16x4_f32 v[182:185], v198, v60, 0
	v_pk_fma_f32 v[52:53], v[16:17], v[52:53], v[150:151]
	v_mfma_f32_16x16x4_f32 v[186:189], v198, v61, 0
	s_waitcnt lgkmcnt(12)
	v_pk_fma_f32 v[152:153], v[18:19], v[52:53], v[152:153] op_sel:[0,1,0] op_sel_hi:[1,0,1]
	v_mfma_f32_16x16x4_f32 v[190:193], v198, v62, 0
	v_pk_fma_f32 v[52:53], v[16:17], v[52:53], v[152:153]
	v_mfma_f32_16x16x4_f32 v[194:197], v198, v63, 0
	s_waitcnt lgkmcnt(11)
	v_pk_fma_f32 v[154:155], v[18:19], v[52:53], v[154:155] op_sel:[0,1,0] op_sel_hi:[1,0,1]
	v_mfma_f32_16x16x4_f32 v[124:127], v199, v64, v[124:127]
	v_pk_fma_f32 v[52:53], v[16:17], v[52:53], v[154:155]
	v_mfma_f32_16x16x4_f32 v[128:131], v199, v65, v[128:131]
	s_waitcnt lgkmcnt(10)
	v_pk_fma_f32 v[156:157], v[18:19], v[52:53], v[156:157] op_sel:[0,1,0] op_sel_hi:[1,0,1]
	v_mfma_f32_16x16x4_f32 v[132:135], v199, v66, v[132:135]
	v_pk_fma_f32 v[52:53], v[16:17], v[52:53], v[156:157]
	v_mfma_f32_16x16x4_f32 v[178:181], v199, v67, v[178:181]
	s_waitcnt lgkmcnt(9)
	v_pk_fma_f32 v[158:159], v[18:19], v[52:53], v[158:159] op_sel:[0,1,0] op_sel_hi:[1,0,1]
	v_mfma_f32_16x16x4_f32 v[182:185], v199, v68, v[182:185]
	v_pk_fma_f32 v[52:53], v[16:17], v[52:53], v[158:159]
	v_mfma_f32_16x16x4_f32 v[186:189], v199, v69, v[186:189]
	s_waitcnt lgkmcnt(8)
	v_pk_fma_f32 v[160:161], v[18:19], v[52:53], v[160:161] op_sel:[0,1,0] op_sel_hi:[1,0,1]
	v_mfma_f32_16x16x4_f32 v[190:193], v199, v70, v[190:193]
	v_pk_fma_f32 v[52:53], v[16:17], v[52:53], v[160:161]
	v_mfma_f32_16x16x4_f32 v[194:197], v199, v71, v[194:197]
	s_waitcnt lgkmcnt(7)
	v_pk_fma_f32 v[162:163], v[18:19], v[52:53], v[162:163] op_sel:[0,1,0] op_sel_hi:[1,0,1]
	v_mfma_f32_16x16x4_f32 v[124:127], v200, v72, v[124:127]
	v_pk_fma_f32 v[52:53], v[16:17], v[52:53], v[162:163]
	v_mfma_f32_16x16x4_f32 v[128:131], v200, v73, v[128:131]
	s_waitcnt lgkmcnt(6)
	v_pk_fma_f32 v[164:165], v[18:19], v[52:53], v[164:165] op_sel:[0,1,0] op_sel_hi:[1,0,1]
	v_mfma_f32_16x16x4_f32 v[132:135], v200, v74, v[132:135]
	v_pk_fma_f32 v[52:53], v[16:17], v[52:53], v[164:165]
	v_mfma_f32_16x16x4_f32 v[178:181], v200, v75, v[178:181]
	s_waitcnt lgkmcnt(5)
	v_pk_fma_f32 v[166:167], v[18:19], v[52:53], v[166:167] op_sel:[0,1,0] op_sel_hi:[1,0,1]
	v_mfma_f32_16x16x4_f32 v[182:185], v200, v76, v[182:185]
	v_pk_fma_f32 v[52:53], v[16:17], v[52:53], v[166:167]
	v_mfma_f32_16x16x4_f32 v[186:189], v200, v77, v[186:189]
	s_waitcnt lgkmcnt(4)
	v_pk_fma_f32 v[168:169], v[18:19], v[52:53], v[168:169] op_sel:[0,1,0] op_sel_hi:[1,0,1]
	v_mfma_f32_16x16x4_f32 v[190:193], v200, v78, v[190:193]
	v_pk_fma_f32 v[52:53], v[16:17], v[52:53], v[168:169]
	v_mfma_f32_16x16x4_f32 v[194:197], v200, v79, v[194:197]
	s_waitcnt lgkmcnt(3)
	v_pk_fma_f32 v[170:171], v[18:19], v[52:53], v[170:171] op_sel:[0,1,0] op_sel_hi:[1,0,1]
	v_mfma_f32_16x16x4_f32 v[124:127], v201, v80, v[124:127]
	v_pk_fma_f32 v[52:53], v[16:17], v[52:53], v[170:171]
	v_mfma_f32_16x16x4_f32 v[128:131], v201, v81, v[128:131]
	s_waitcnt lgkmcnt(2)
	v_pk_fma_f32 v[172:173], v[18:19], v[52:53], v[172:173] op_sel:[0,1,0] op_sel_hi:[1,0,1]
	v_mfma_f32_16x16x4_f32 v[132:135], v201, v82, v[132:135]
	v_pk_fma_f32 v[52:53], v[16:17], v[52:53], v[172:173]
	v_mfma_f32_16x16x4_f32 v[178:181], v201, v83, v[178:181]
	s_waitcnt lgkmcnt(1)
	v_pk_fma_f32 v[174:175], v[18:19], v[52:53], v[174:175] op_sel:[0,1,0] op_sel_hi:[1,0,1]
	v_mfma_f32_16x16x4_f32 v[182:185], v201, v84, v[182:185]
	v_pk_fma_f32 v[52:53], v[16:17], v[52:53], v[174:175]
	v_mfma_f32_16x16x4_f32 v[186:189], v201, v85, v[186:189]
	s_waitcnt lgkmcnt(0)
	v_pk_fma_f32 v[176:177], v[18:19], v[52:53], v[176:177] op_sel:[0,1,0] op_sel_hi:[1,0,1]
	v_mfma_f32_16x16x4_f32 v[190:193], v201, v86, v[190:193]
	v_pk_fma_f32 v[52:53], v[16:17], v[52:53], v[176:177]
	v_mfma_f32_16x16x4_f32 v[194:197], v201, v87, v[194:197]
	s_nop 15
	s_nop 7
	ds_write_b32 v142, v124
	ds_write_b32 v142, v125 offset:528
	ds_write_b32 v142, v126 offset:1056
	ds_write_b32 v142, v127 offset:1584
	ds_write_b32 v142, v128 offset:64
	ds_write_b32 v142, v129 offset:592
	ds_write_b32 v142, v130 offset:1120
	ds_write_b32 v142, v131 offset:1648
	ds_write_b32 v142, v132 offset:128
	ds_write_b32 v142, v133 offset:656
	ds_write_b32 v142, v134 offset:1184
	ds_write_b32 v142, v135 offset:1712
	ds_write_b32 v142, v178 offset:192
	ds_write_b32 v142, v179 offset:720
	ds_write_b32 v142, v180 offset:1248
	ds_write_b32 v142, v181 offset:1776
	ds_write_b32 v142, v182 offset:256
	ds_write_b32 v142, v183 offset:784
	ds_write_b32 v142, v184 offset:1312
	ds_write_b32 v142, v185 offset:1840
	ds_write_b32 v142, v186 offset:320
	ds_write_b32 v142, v187 offset:848
	ds_write_b32 v142, v188 offset:1376
	ds_write_b32 v142, v189 offset:1904
	ds_write_b32 v142, v190 offset:384
	ds_write_b32 v142, v191 offset:912
	ds_write_b32 v142, v192 offset:1440
	ds_write_b32 v142, v193 offset:1968
	ds_write_b32 v142, v194 offset:448
	ds_write_b32 v142, v195 offset:976
	ds_write_b32 v142, v196 offset:1504
	ds_write_b32 v142, v197 offset:2032
	ds_read_b32 v88, v143 offset:2048
	ds_read_b32 v89, v143 offset:2064
	ds_read_b32 v90, v143 offset:2080
	ds_read_b32 v91, v143 offset:2096
	s_waitcnt lgkmcnt(0)
	ds_read_b64 v[146:147], v140
	ds_read_b64 v[148:149], v140 offset:528
	ds_read_b64 v[150:151], v140 offset:1056
	ds_read_b64 v[152:153], v140 offset:1584
	ds_read_b64 v[154:155], v140 offset:2112
	ds_read_b64 v[156:157], v140 offset:2640
	ds_read_b64 v[158:159], v140 offset:3168
	ds_read_b64 v[160:161], v140 offset:3696
	ds_read_b64 v[162:163], v140 offset:4224
	ds_read_b64 v[164:165], v140 offset:4752
	ds_read_b64 v[166:167], v140 offset:5280
	ds_read_b64 v[168:169], v140 offset:5808
	ds_read_b64 v[170:171], v140 offset:6336
	ds_read_b64 v[172:173], v140 offset:6864
	ds_read_b64 v[174:175], v140 offset:7392
	ds_read_b64 v[176:177], v140 offset:7920
	s_waitcnt lgkmcnt(15)
	v_pk_fma_f32 v[146:147], v[18:19], v[52:53], v[146:147] op_sel:[0,1,0] op_sel_hi:[1,0,1]
	v_mfma_f32_16x16x4_f32 v[92:95], v88, v56, 0
	v_pk_fma_f32 v[52:53], v[16:17], v[52:53], v[146:147]
	v_mfma_f32_16x16x4_f32 v[96:99], v88, v57, 0
	s_waitcnt lgkmcnt(14)
	v_pk_fma_f32 v[148:149], v[18:19], v[52:53], v[148:149] op_sel:[0,1,0] op_sel_hi:[1,0,1]
	v_mfma_f32_16x16x4_f32 v[100:103], v88, v58, 0
	v_pk_fma_f32 v[52:53], v[16:17], v[52:53], v[148:149]
	v_mfma_f32_16x16x4_f32 v[104:107], v88, v59, 0
	s_waitcnt lgkmcnt(13)
	v_pk_fma_f32 v[150:151], v[18:19], v[52:53], v[150:151] op_sel:[0,1,0] op_sel_hi:[1,0,1]
	v_mfma_f32_16x16x4_f32 v[108:111], v88, v60, 0
	v_pk_fma_f32 v[52:53], v[16:17], v[52:53], v[150:151]
	v_mfma_f32_16x16x4_f32 v[112:115], v88, v61, 0
	s_waitcnt lgkmcnt(12)
	v_pk_fma_f32 v[152:153], v[18:19], v[52:53], v[152:153] op_sel:[0,1,0] op_sel_hi:[1,0,1]
	v_mfma_f32_16x16x4_f32 v[116:119], v88, v62, 0
	v_pk_fma_f32 v[52:53], v[16:17], v[52:53], v[152:153]
	v_mfma_f32_16x16x4_f32 v[120:123], v88, v63, 0
	s_waitcnt lgkmcnt(11)
	v_pk_fma_f32 v[154:155], v[18:19], v[52:53], v[154:155] op_sel:[0,1,0] op_sel_hi:[1,0,1]
	v_mfma_f32_16x16x4_f32 v[92:95], v89, v64, v[92:95]
	v_pk_fma_f32 v[52:53], v[16:17], v[52:53], v[154:155]
	v_mfma_f32_16x16x4_f32 v[96:99], v89, v65, v[96:99]
	s_waitcnt lgkmcnt(10)
	v_pk_fma_f32 v[156:157], v[18:19], v[52:53], v[156:157] op_sel:[0,1,0] op_sel_hi:[1,0,1]
	v_mfma_f32_16x16x4_f32 v[100:103], v89, v66, v[100:103]
	v_pk_fma_f32 v[52:53], v[16:17], v[52:53], v[156:157]
	v_mfma_f32_16x16x4_f32 v[104:107], v89, v67, v[104:107]
	s_waitcnt lgkmcnt(9)
	v_pk_fma_f32 v[158:159], v[18:19], v[52:53], v[158:159] op_sel:[0,1,0] op_sel_hi:[1,0,1]
	v_mfma_f32_16x16x4_f32 v[108:111], v89, v68, v[108:111]
	v_pk_fma_f32 v[52:53], v[16:17], v[52:53], v[158:159]
	v_mfma_f32_16x16x4_f32 v[112:115], v89, v69, v[112:115]
	s_waitcnt lgkmcnt(8)
	v_pk_fma_f32 v[160:161], v[18:19], v[52:53], v[160:161] op_sel:[0,1,0] op_sel_hi:[1,0,1]
	v_mfma_f32_16x16x4_f32 v[116:119], v89, v70, v[116:119]
	v_pk_fma_f32 v[52:53], v[16:17], v[52:53], v[160:161]
	v_mfma_f32_16x16x4_f32 v[120:123], v89, v71, v[120:123]
	s_waitcnt lgkmcnt(7)
	v_pk_fma_f32 v[162:163], v[18:19], v[52:53], v[162:163] op_sel:[0,1,0] op_sel_hi:[1,0,1]
	v_mfma_f32_16x16x4_f32 v[92:95], v90, v72, v[92:95]
	v_pk_fma_f32 v[52:53], v[16:17], v[52:53], v[162:163]
	v_mfma_f32_16x16x4_f32 v[96:99], v90, v73, v[96:99]
	s_waitcnt lgkmcnt(6)
	v_pk_fma_f32 v[164:165], v[18:19], v[52:53], v[164:165] op_sel:[0,1,0] op_sel_hi:[1,0,1]
	v_mfma_f32_16x16x4_f32 v[100:103], v90, v74, v[100:103]
	v_pk_fma_f32 v[52:53], v[16:17], v[52:53], v[164:165]
	v_mfma_f32_16x16x4_f32 v[104:107], v90, v75, v[104:107]
	s_waitcnt lgkmcnt(5)
	v_pk_fma_f32 v[166:167], v[18:19], v[52:53], v[166:167] op_sel:[0,1,0] op_sel_hi:[1,0,1]
	v_mfma_f32_16x16x4_f32 v[108:111], v90, v76, v[108:111]
	v_pk_fma_f32 v[52:53], v[16:17], v[52:53], v[166:167]
	v_mfma_f32_16x16x4_f32 v[112:115], v90, v77, v[112:115]
	s_waitcnt lgkmcnt(4)
	v_pk_fma_f32 v[168:169], v[18:19], v[52:53], v[168:169] op_sel:[0,1,0] op_sel_hi:[1,0,1]
	v_mfma_f32_16x16x4_f32 v[116:119], v90, v78, v[116:119]
	v_pk_fma_f32 v[52:53], v[16:17], v[52:53], v[168:169]
	v_mfma_f32_16x16x4_f32 v[120:123], v90, v79, v[120:123]
	s_waitcnt lgkmcnt(3)
	v_pk_fma_f32 v[170:171], v[18:19], v[52:53], v[170:171] op_sel:[0,1,0] op_sel_hi:[1,0,1]
	v_mfma_f32_16x16x4_f32 v[92:95], v91, v80, v[92:95]
	v_pk_fma_f32 v[52:53], v[16:17], v[52:53], v[170:171]
	v_mfma_f32_16x16x4_f32 v[96:99], v91, v81, v[96:99]
	s_waitcnt lgkmcnt(2)
	v_pk_fma_f32 v[172:173], v[18:19], v[52:53], v[172:173] op_sel:[0,1,0] op_sel_hi:[1,0,1]
	v_mfma_f32_16x16x4_f32 v[100:103], v91, v82, v[100:103]
	v_pk_fma_f32 v[52:53], v[16:17], v[52:53], v[172:173]
	v_mfma_f32_16x16x4_f32 v[104:107], v91, v83, v[104:107]
	s_waitcnt lgkmcnt(1)
	v_pk_fma_f32 v[174:175], v[18:19], v[52:53], v[174:175] op_sel:[0,1,0] op_sel_hi:[1,0,1]
	v_mfma_f32_16x16x4_f32 v[108:111], v91, v84, v[108:111]
	v_pk_fma_f32 v[52:53], v[16:17], v[52:53], v[174:175]
	v_mfma_f32_16x16x4_f32 v[112:115], v91, v85, v[112:115]
	s_waitcnt lgkmcnt(0)
	v_pk_fma_f32 v[176:177], v[18:19], v[52:53], v[176:177] op_sel:[0,1,0] op_sel_hi:[1,0,1]
	v_mfma_f32_16x16x4_f32 v[116:119], v91, v86, v[116:119]
	v_pk_fma_f32 v[52:53], v[16:17], v[52:53], v[176:177]
	v_mfma_f32_16x16x4_f32 v[120:123], v91, v87, v[120:123]
	s_nop 15
	s_nop 7
	ds_write_b32 v142, v92
	ds_write_b32 v142, v93 offset:528
	ds_write_b32 v142, v94 offset:1056
	ds_write_b32 v142, v95 offset:1584
	ds_write_b32 v142, v96 offset:64
	ds_write_b32 v142, v97 offset:592
	ds_write_b32 v142, v98 offset:1120
	ds_write_b32 v142, v99 offset:1648
	ds_write_b32 v142, v100 offset:128
	ds_write_b32 v142, v101 offset:656
	ds_write_b32 v142, v102 offset:1184
	ds_write_b32 v142, v103 offset:1712
	ds_write_b32 v142, v104 offset:192
	ds_write_b32 v142, v105 offset:720
	ds_write_b32 v142, v106 offset:1248
	ds_write_b32 v142, v107 offset:1776
	ds_write_b32 v142, v108 offset:256
	ds_write_b32 v142, v109 offset:784
	ds_write_b32 v142, v110 offset:1312
	ds_write_b32 v142, v111 offset:1840
	ds_write_b32 v142, v112 offset:320
	ds_write_b32 v142, v113 offset:848
	ds_write_b32 v142, v114 offset:1376
	ds_write_b32 v142, v115 offset:1904
	ds_write_b32 v142, v116 offset:384
	ds_write_b32 v142, v117 offset:912
	ds_write_b32 v142, v118 offset:1440
	ds_write_b32 v142, v119 offset:1968
	ds_write_b32 v142, v120 offset:448
	ds_write_b32 v142, v121 offset:976
	ds_write_b32 v142, v122 offset:1504
	ds_write_b32 v142, v123 offset:2032
	ds_read_b32 v198, v143 offset:3072
	ds_read_b32 v199, v143 offset:3088
	ds_read_b32 v200, v143 offset:3104
	ds_read_b32 v201, v143 offset:3120
	s_waitcnt lgkmcnt(0)
	ds_read_b64 v[146:147], v140
	ds_read_b64 v[148:149], v140 offset:528
	ds_read_b64 v[150:151], v140 offset:1056
	ds_read_b64 v[152:153], v140 offset:1584
	ds_read_b64 v[154:155], v140 offset:2112
	ds_read_b64 v[156:157], v140 offset:2640
	ds_read_b64 v[158:159], v140 offset:3168
	ds_read_b64 v[160:161], v140 offset:3696
	ds_read_b64 v[162:163], v140 offset:4224
	ds_read_b64 v[164:165], v140 offset:4752
	ds_read_b64 v[166:167], v140 offset:5280
	ds_read_b64 v[168:169], v140 offset:5808
	ds_read_b64 v[170:171], v140 offset:6336
	ds_read_b64 v[172:173], v140 offset:6864
	ds_read_b64 v[174:175], v140 offset:7392
	ds_read_b64 v[176:177], v140 offset:7920
	s_waitcnt lgkmcnt(15)
	v_pk_fma_f32 v[146:147], v[18:19], v[52:53], v[146:147] op_sel:[0,1,0] op_sel_hi:[1,0,1]
	v_mfma_f32_16x16x4_f32 v[124:127], v198, v56, 0
	v_pk_fma_f32 v[52:53], v[16:17], v[52:53], v[146:147]
	v_mfma_f32_16x16x4_f32 v[128:131], v198, v57, 0
	s_waitcnt lgkmcnt(14)
	v_pk_fma_f32 v[148:149], v[18:19], v[52:53], v[148:149] op_sel:[0,1,0] op_sel_hi:[1,0,1]
	v_mfma_f32_16x16x4_f32 v[132:135], v198, v58, 0
	v_pk_fma_f32 v[52:53], v[16:17], v[52:53], v[148:149]
	v_mfma_f32_16x16x4_f32 v[178:181], v198, v59, 0
	s_waitcnt lgkmcnt(13)
	v_pk_fma_f32 v[150:151], v[18:19], v[52:53], v[150:151] op_sel:[0,1,0] op_sel_hi:[1,0,1]
	v_mfma_f32_16x16x4_f32 v[182:185], v198, v60, 0
	v_pk_fma_f32 v[52:53], v[16:17], v[52:53], v[150:151]
	v_mfma_f32_16x16x4_f32 v[186:189], v198, v61, 0
	s_waitcnt lgkmcnt(12)
	v_pk_fma_f32 v[152:153], v[18:19], v[52:53], v[152:153] op_sel:[0,1,0] op_sel_hi:[1,0,1]
	v_mfma_f32_16x16x4_f32 v[190:193], v198, v62, 0
	v_pk_fma_f32 v[52:53], v[16:17], v[52:53], v[152:153]
	v_mfma_f32_16x16x4_f32 v[194:197], v198, v63, 0
	s_waitcnt lgkmcnt(11)
	v_pk_fma_f32 v[154:155], v[18:19], v[52:53], v[154:155] op_sel:[0,1,0] op_sel_hi:[1,0,1]
	v_mfma_f32_16x16x4_f32 v[124:127], v199, v64, v[124:127]
	v_pk_fma_f32 v[52:53], v[16:17], v[52:53], v[154:155]
	v_mfma_f32_16x16x4_f32 v[128:131], v199, v65, v[128:131]
	s_waitcnt lgkmcnt(10)
	v_pk_fma_f32 v[156:157], v[18:19], v[52:53], v[156:157] op_sel:[0,1,0] op_sel_hi:[1,0,1]
	v_mfma_f32_16x16x4_f32 v[132:135], v199, v66, v[132:135]
	v_pk_fma_f32 v[52:53], v[16:17], v[52:53], v[156:157]
	v_mfma_f32_16x16x4_f32 v[178:181], v199, v67, v[178:181]
	s_waitcnt lgkmcnt(9)
	v_pk_fma_f32 v[158:159], v[18:19], v[52:53], v[158:159] op_sel:[0,1,0] op_sel_hi:[1,0,1]
	v_mfma_f32_16x16x4_f32 v[182:185], v199, v68, v[182:185]
	v_pk_fma_f32 v[52:53], v[16:17], v[52:53], v[158:159]
	v_mfma_f32_16x16x4_f32 v[186:189], v199, v69, v[186:189]
	s_waitcnt lgkmcnt(8)
	v_pk_fma_f32 v[160:161], v[18:19], v[52:53], v[160:161] op_sel:[0,1,0] op_sel_hi:[1,0,1]
	v_mfma_f32_16x16x4_f32 v[190:193], v199, v70, v[190:193]
	v_pk_fma_f32 v[52:53], v[16:17], v[52:53], v[160:161]
	v_mfma_f32_16x16x4_f32 v[194:197], v199, v71, v[194:197]
	s_waitcnt lgkmcnt(7)
	v_pk_fma_f32 v[162:163], v[18:19], v[52:53], v[162:163] op_sel:[0,1,0] op_sel_hi:[1,0,1]
	v_mfma_f32_16x16x4_f32 v[124:127], v200, v72, v[124:127]
	v_pk_fma_f32 v[52:53], v[16:17], v[52:53], v[162:163]
	v_mfma_f32_16x16x4_f32 v[128:131], v200, v73, v[128:131]
	s_waitcnt lgkmcnt(6)
	v_pk_fma_f32 v[164:165], v[18:19], v[52:53], v[164:165] op_sel:[0,1,0] op_sel_hi:[1,0,1]
	v_mfma_f32_16x16x4_f32 v[132:135], v200, v74, v[132:135]
	v_pk_fma_f32 v[52:53], v[16:17], v[52:53], v[164:165]
	v_mfma_f32_16x16x4_f32 v[178:181], v200, v75, v[178:181]
	s_waitcnt lgkmcnt(5)
	v_pk_fma_f32 v[166:167], v[18:19], v[52:53], v[166:167] op_sel:[0,1,0] op_sel_hi:[1,0,1]
	v_mfma_f32_16x16x4_f32 v[182:185], v200, v76, v[182:185]
	v_pk_fma_f32 v[52:53], v[16:17], v[52:53], v[166:167]
	v_mfma_f32_16x16x4_f32 v[186:189], v200, v77, v[186:189]
	s_waitcnt lgkmcnt(4)
	v_pk_fma_f32 v[168:169], v[18:19], v[52:53], v[168:169] op_sel:[0,1,0] op_sel_hi:[1,0,1]
	v_mfma_f32_16x16x4_f32 v[190:193], v200, v78, v[190:193]
	v_pk_fma_f32 v[52:53], v[16:17], v[52:53], v[168:169]
	v_mfma_f32_16x16x4_f32 v[194:197], v200, v79, v[194:197]
	s_waitcnt lgkmcnt(3)
	v_pk_fma_f32 v[170:171], v[18:19], v[52:53], v[170:171] op_sel:[0,1,0] op_sel_hi:[1,0,1]
	v_mfma_f32_16x16x4_f32 v[124:127], v201, v80, v[124:127]
	v_pk_fma_f32 v[52:53], v[16:17], v[52:53], v[170:171]
	v_mfma_f32_16x16x4_f32 v[128:131], v201, v81, v[128:131]
	s_waitcnt lgkmcnt(2)
	v_pk_fma_f32 v[172:173], v[18:19], v[52:53], v[172:173] op_sel:[0,1,0] op_sel_hi:[1,0,1]
	v_mfma_f32_16x16x4_f32 v[132:135], v201, v82, v[132:135]
	v_pk_fma_f32 v[52:53], v[16:17], v[52:53], v[172:173]
	v_mfma_f32_16x16x4_f32 v[178:181], v201, v83, v[178:181]
	s_waitcnt lgkmcnt(1)
	v_pk_fma_f32 v[174:175], v[18:19], v[52:53], v[174:175] op_sel:[0,1,0] op_sel_hi:[1,0,1]
	v_mfma_f32_16x16x4_f32 v[182:185], v201, v84, v[182:185]
	v_pk_fma_f32 v[52:53], v[16:17], v[52:53], v[174:175]
	v_mfma_f32_16x16x4_f32 v[186:189], v201, v85, v[186:189]
	s_waitcnt lgkmcnt(0)
	v_pk_fma_f32 v[176:177], v[18:19], v[52:53], v[176:177] op_sel:[0,1,0] op_sel_hi:[1,0,1]
	v_mfma_f32_16x16x4_f32 v[190:193], v201, v86, v[190:193]
	v_pk_fma_f32 v[52:53], v[16:17], v[52:53], v[176:177]
	v_mfma_f32_16x16x4_f32 v[194:197], v201, v87, v[194:197]
	s_nop 15
	s_nop 7
	ds_write_b32 v142, v124
	ds_write_b32 v142, v125 offset:528
	ds_write_b32 v142, v126 offset:1056
	ds_write_b32 v142, v127 offset:1584
	ds_write_b32 v142, v128 offset:64
	ds_write_b32 v142, v129 offset:592
	ds_write_b32 v142, v130 offset:1120
	ds_write_b32 v142, v131 offset:1648
	ds_write_b32 v142, v132 offset:128
	ds_write_b32 v142, v133 offset:656
	ds_write_b32 v142, v134 offset:1184
	ds_write_b32 v142, v135 offset:1712
	ds_write_b32 v142, v178 offset:192
	ds_write_b32 v142, v179 offset:720
	ds_write_b32 v142, v180 offset:1248
	ds_write_b32 v142, v181 offset:1776
	ds_write_b32 v142, v182 offset:256
	ds_write_b32 v142, v183 offset:784
	ds_write_b32 v142, v184 offset:1312
	ds_write_b32 v142, v185 offset:1840
	ds_write_b32 v142, v186 offset:320
	ds_write_b32 v142, v187 offset:848
	ds_write_b32 v142, v188 offset:1376
	ds_write_b32 v142, v189 offset:1904
	ds_write_b32 v142, v190 offset:384
	ds_write_b32 v142, v191 offset:912
	ds_write_b32 v142, v192 offset:1440
	ds_write_b32 v142, v193 offset:1968
	ds_write_b32 v142, v194 offset:448
	ds_write_b32 v142, v195 offset:976
	ds_write_b32 v142, v196 offset:1504
	ds_write_b32 v142, v197 offset:2032
	s_waitcnt lgkmcnt(0)
	ds_read_b64 v[146:147], v140
	ds_read_b64 v[148:149], v140 offset:528
	ds_read_b64 v[150:151], v140 offset:1056
	ds_read_b64 v[152:153], v140 offset:1584
	ds_read_b64 v[154:155], v140 offset:2112
	ds_read_b64 v[156:157], v140 offset:2640
	ds_read_b64 v[158:159], v140 offset:3168
	ds_read_b64 v[160:161], v140 offset:3696
	ds_read_b64 v[162:163], v140 offset:4224
	ds_read_b64 v[164:165], v140 offset:4752
	ds_read_b64 v[166:167], v140 offset:5280
	ds_read_b64 v[168:169], v140 offset:5808
	ds_read_b64 v[170:171], v140 offset:6336
	ds_read_b64 v[172:173], v140 offset:6864
	ds_read_b64 v[174:175], v140 offset:7392
	ds_read_b64 v[176:177], v140 offset:7920
	s_waitcnt lgkmcnt(15)
	v_pk_fma_f32 v[146:147], v[18:19], v[52:53], v[146:147] op_sel:[0,1,0] op_sel_hi:[1,0,1]
	s_nop 0
	v_pk_fma_f32 v[52:53], v[16:17], v[52:53], v[146:147]
	s_nop 0
	s_waitcnt lgkmcnt(14)
	v_pk_fma_f32 v[148:149], v[18:19], v[52:53], v[148:149] op_sel:[0,1,0] op_sel_hi:[1,0,1]
	s_nop 0
	v_pk_fma_f32 v[52:53], v[16:17], v[52:53], v[148:149]
	s_nop 0
	s_waitcnt lgkmcnt(13)
	v_pk_fma_f32 v[150:151], v[18:19], v[52:53], v[150:151] op_sel:[0,1,0] op_sel_hi:[1,0,1]
	s_nop 0
	v_pk_fma_f32 v[52:53], v[16:17], v[52:53], v[150:151]
	s_nop 0
	s_waitcnt lgkmcnt(12)
	v_pk_fma_f32 v[152:153], v[18:19], v[52:53], v[152:153] op_sel:[0,1,0] op_sel_hi:[1,0,1]
	s_nop 0
	v_pk_fma_f32 v[52:53], v[16:17], v[52:53], v[152:153]
	s_nop 0
	s_waitcnt lgkmcnt(11)
	v_pk_fma_f32 v[154:155], v[18:19], v[52:53], v[154:155] op_sel:[0,1,0] op_sel_hi:[1,0,1]
	s_nop 0
	v_pk_fma_f32 v[52:53], v[16:17], v[52:53], v[154:155]
	s_nop 0
	s_waitcnt lgkmcnt(10)
	v_pk_fma_f32 v[156:157], v[18:19], v[52:53], v[156:157] op_sel:[0,1,0] op_sel_hi:[1,0,1]
	s_nop 0
	v_pk_fma_f32 v[52:53], v[16:17], v[52:53], v[156:157]
	s_nop 0
	s_waitcnt lgkmcnt(9)
	v_pk_fma_f32 v[158:159], v[18:19], v[52:53], v[158:159] op_sel:[0,1,0] op_sel_hi:[1,0,1]
	s_nop 0
	v_pk_fma_f32 v[52:53], v[16:17], v[52:53], v[158:159]
	s_nop 0
	s_waitcnt lgkmcnt(8)
	v_pk_fma_f32 v[160:161], v[18:19], v[52:53], v[160:161] op_sel:[0,1,0] op_sel_hi:[1,0,1]
	s_nop 0
	v_pk_fma_f32 v[52:53], v[16:17], v[52:53], v[160:161]
	s_nop 0
	s_waitcnt lgkmcnt(7)
	v_pk_fma_f32 v[162:163], v[18:19], v[52:53], v[162:163] op_sel:[0,1,0] op_sel_hi:[1,0,1]
	s_nop 0
	v_pk_fma_f32 v[52:53], v[16:17], v[52:53], v[162:163]
	s_nop 0
	s_waitcnt lgkmcnt(6)
	v_pk_fma_f32 v[164:165], v[18:19], v[52:53], v[164:165] op_sel:[0,1,0] op_sel_hi:[1,0,1]
	s_nop 0
	v_pk_fma_f32 v[52:53], v[16:17], v[52:53], v[164:165]
	s_nop 0
	s_waitcnt lgkmcnt(5)
	v_pk_fma_f32 v[166:167], v[18:19], v[52:53], v[166:167] op_sel:[0,1,0] op_sel_hi:[1,0,1]
	s_nop 0
	v_pk_fma_f32 v[52:53], v[16:17], v[52:53], v[166:167]
	s_nop 0
	s_waitcnt lgkmcnt(4)
	v_pk_fma_f32 v[168:169], v[18:19], v[52:53], v[168:169] op_sel:[0,1,0] op_sel_hi:[1,0,1]
	s_nop 0
	v_pk_fma_f32 v[52:53], v[16:17], v[52:53], v[168:169]
	s_nop 0
	s_waitcnt lgkmcnt(3)
	v_pk_fma_f32 v[170:171], v[18:19], v[52:53], v[170:171] op_sel:[0,1,0] op_sel_hi:[1,0,1]
	s_nop 0
	v_pk_fma_f32 v[52:53], v[16:17], v[52:53], v[170:171]
	s_nop 0
	s_waitcnt lgkmcnt(2)
	v_pk_fma_f32 v[172:173], v[18:19], v[52:53], v[172:173] op_sel:[0,1,0] op_sel_hi:[1,0,1]
	s_nop 0
	v_pk_fma_f32 v[52:53], v[16:17], v[52:53], v[172:173]
	s_nop 0
	s_waitcnt lgkmcnt(1)
	v_pk_fma_f32 v[174:175], v[18:19], v[52:53], v[174:175] op_sel:[0,1,0] op_sel_hi:[1,0,1]
	s_nop 0
	v_pk_fma_f32 v[52:53], v[16:17], v[52:53], v[174:175]
	s_nop 0
	s_waitcnt lgkmcnt(0)
	v_pk_fma_f32 v[176:177], v[18:19], v[52:53], v[176:177] op_sel:[0,1,0] op_sel_hi:[1,0,1]
	s_nop 0
	v_pk_fma_f32 v[52:53], v[16:17], v[52:53], v[176:177]
	s_nop 0
	v_ashrrev_i32_e32 v13, 31, v12
	v_lshlrev_b64 v[0:1], 14, v[12:13]
	v_lshl_add_u64 v[0:1], s[22:23], 0, v[0:1]
	v_lshlrev_b64 v[2:3], 9, v[14:15]
	v_lshl_add_u64 v[0:1], v[0:1], 0, v[2:3]
	s_waitcnt lgkmcnt(0)
	v_lshl_add_u64 v[0:1], v[0:1], 0, v[144:145]
	s_movk_i32 s0, 0x5ff
	global_store_dword v[0:1], v53, off
	global_store_dword v[0:1], v52, off offset:256
	s_cmp_lg_u32 s30, 1
	s_cbranch_scc1 .LBB0_308
	s_mov_b32 s30, 2
	v_add_u32_e32 v12, 56, v12
	s_mov_b32 s6, 0x20c0000
	s_mov_b32 s7, 0
	v_lshl_add_u64 v[202:203], s[6:7], 0, v[202:203]
	global_load_dwordx4 v[128:131], v[202:203], off offset:2688
	global_load_dwordx4 v[132:135], v[202:203], off offset:2704
	v_mov_b64_e32 v[52:53], 0
	s_branch .Lssml_stage
